# M8: M2 + s_setprio 2 on the baseline K2's eight consumer waves
# speedup vs baseline: 1.0456x; 1.0456x over previous
_Z11attn_kernelPKiPKDv8_DF16_PKDF16_S5_PDF16_Pf:
	s_mul_i32 s3, s2, 27
	s_mul_hi_i32 s26, s3, 0x2aaaaaab
	v_and_b32_e32 v102, 63, v0
	s_lshr_b32 s27, s26, 31
	s_ashr_i32 s28, s26, 3
	s_movk_i32 s4, 0x200
	v_lshrrev_b32_e32 v98, 6, v0
	s_add_i32 s28, s28, s27
	v_cmp_gt_u32_e32 vcc, s4, v0
	s_mul_hi_i32 s29, s3, 0x38e38e39
	v_lshlrev_b32_e32 v122, 4, v102
	s_and_saveexec_b64 s[4:5], vcc
	s_xor_b64 s[12:13], exec, s[4:5]
	s_cbranch_execz .LBB1_65
	s_setprio 2
	s_lshr_b32 s6, s29, 31
	s_ashr_i32 s7, s29, 9
	s_add_i32 s6, s7, s6
	s_mul_i32 s7, s6, 0xffffffd0
	v_bfe_u32 v117, v0, 6, 2
	s_add_i32 s7, s7, s28
	v_lshl_or_b32 v4, s6, 2, v117
	s_lshl_b32 s6, s7, 6
	s_load_dwordx2 s[4:5], s[0:1], 0x8
	s_load_dwordx4 s[8:11], s[0:1], 0x18
	s_load_dwordx2 s[14:15], s[0:1], 0x28
	s_movk_i32 s30, 0xc00
	v_mov_b32_e32 v2, s6
	v_and_b32_e32 v119, 31, v0
	v_mad_i32_i24 v2, v4, s30, v2
	v_or_b32_e32 v2, v2, v119
	s_mul_i32 s6, s28, 48
	v_ashrrev_i32_e32 v3, 31, v2
	s_sub_i32 s6, s3, s6
	s_waitcnt lgkmcnt(0)
	v_lshl_add_u64 v[2:3], v[2:3], 1, s[8:9]
	s_lshl_b32 s6, s6, 2
	global_load_ushort v5, v[2:3], off
	global_load_ushort v6, v[2:3], off offset:64
	s_movk_i32 s31, 0xc0
	v_mov_b32_e32 v2, s6
	s_add_i32 s6, s3, 1
	v_mad_i32_i24 v2, v4, s31, v2
	v_lshrrev_b32_e32 v4, 7, v0
	s_mul_hi_i32 s7, s6, 0x2aaaaaab
	v_and_b32_e32 v121, 2, v4
	s_lshr_b32 s16, s7, 31
	s_lshr_b32 s7, s7, 3
	v_or_b32_e32 v2, v2, v121
	s_add_i32 s7, s7, s16
	v_ashrrev_i32_e32 v3, 31, v2
	s_mul_i32 s7, s7, 48
	v_lshlrev_b64 v[2:3], 11, v[2:3]
	s_sub_i32 s7, s6, s7
	s_mul_hi_i32 s6, s6, 0x38e38e39
	v_lshl_add_u64 v[2:3], s[4:5], 0, v[2:3]
	v_mov_b32_e32 v123, 0
	s_lshr_b32 s16, s6, 31
	s_lshr_b32 s6, s6, 9
	v_lshl_add_u64 v[2:3], v[2:3], 0, v[122:123]
	s_add_i32 s6, s6, s16
	global_load_dwordx4 v[86:89], v[2:3], off
	global_load_dwordx4 v[82:85], v[2:3], off offset:1024
	global_load_dwordx4 v[70:73], v[2:3], off offset:2048
	global_load_dwordx4 v[66:69], v[2:3], off offset:3072
	v_lshl_or_b32 v2, s6, 2, v117
	s_lshl_b32 s6, s7, 2
	v_mov_b32_e32 v3, s6
	v_mad_i32_i24 v2, v2, s31, v3
	v_or_b32_e32 v2, v2, v121
	v_ashrrev_i32_e32 v3, 31, v2
	v_lshlrev_b64 v[2:3], 11, v[2:3]
	v_lshl_add_u64 v[2:3], s[4:5], 0, v[2:3]
	v_lshl_add_u64 v[2:3], v[2:3], 0, v[122:123]
	global_load_dwordx4 v[94:97], v[2:3], off
	global_load_dwordx4 v[90:93], v[2:3], off offset:1024
	global_load_dwordx4 v[78:81], v[2:3], off offset:2048
	global_load_dwordx4 v[74:77], v[2:3], off offset:3072
	v_lshlrev_b32_e32 v3, 2, v102
	v_lshrrev_b32_e32 v1, 5, v102
	v_lshl_add_u64 v[114:115], s[4:5], 0, v[122:123]
	s_movk_i32 s4, 0xff
	v_lshl_or_b32 v127, v117, 14, v3
	v_lshlrev_b32_e32 v3, 8, v117
	v_lshlrev_b32_e32 v7, 2, v119
	s_mov_b32 s16, 0x15000
	v_cmp_lt_u32_e64 s[6:7], s4, v0
	v_or3_b32 v128, v3, v7, s16
	v_lshlrev_b32_e32 v3, 10, v1
	v_and_b32_e32 v0, 0xc0, v0
	v_lshlrev_b32_e32 v2, 1, v117
	v_or3_b32 v124, v3, v0, v119
	v_lshlrev_b32_e32 v0, 3, v121
	v_or3_b32 v0, v2, v0, v1
	v_lshlrev_b32_e32 v8, 6, v117
	v_lshlrev_b32_e32 v129, 5, v0
	v_or_b32_e32 v0, 1, v4
	v_or3_b32 v116, v3, v8, v119
	v_lshlrev_b32_e32 v3, 3, v0
	v_lshlrev_b32_e32 v125, 4, v1
	s_movk_i32 s16, 0x80
	v_or3_b32 v1, v2, v3, v1
	v_lshlrev_b32_e32 v133, 5, v0
	s_mov_b32 s36, 0x5040100
	v_mbcnt_lo_u32_b32 v0, -1, 0
	s_add_i32 s33, s3, 2
	v_cmp_gt_u32_e64 s[4:5], 32, v102
	s_lshl_b32 s34, s2, 1
	s_movk_i32 s35, 0x2000
	v_or_b32_e32 v118, 0x2000, v116
	v_or3_b32 v120, v7, v117, s16
	v_add_u32_e32 v126, v7, v98
	v_lshlrev_b32_e32 v130, 5, v121
	v_mul_u32_u24_e32 v131, 0x90, v119
	v_lshlrev_b32_e32 v132, 5, v1
	s_mov_b32 s42, 0
	s_movk_i32 s37, 0x5000
	s_movk_i32 s38, 0x6000
	s_movk_i32 s39, 0x7000
	s_movk_i32 s40, 0x1000
	s_movk_i32 s41, 0x3000
	v_mbcnt_hi_u32_b32 v134, -1, v0
	v_mov_b32_e32 v1, 0
	s_waitcnt vmcnt(9)
	v_perm_b32 v136, v5, v5, s36
	s_waitcnt vmcnt(8)
	v_perm_b32 v135, v6, v6, s36
	v_mov_b32_e32 v122, 0
	v_mov_b32_e32 v18, v123
	v_mov_b32_e32 v19, v123
	v_mov_b32_e32 v20, v123
	v_mov_b32_e32 v21, v123
	v_mov_b32_e32 v22, v123
	v_mov_b32_e32 v23, v123
	v_mov_b32_e32 v24, v123
	v_mov_b32_e32 v25, v123
	v_mov_b32_e32 v26, v123
	v_mov_b32_e32 v27, v123
	v_mov_b32_e32 v28, v123
	v_mov_b32_e32 v29, v123
	v_mov_b32_e32 v30, v123
	v_mov_b32_e32 v31, v123
	v_mov_b32_e32 v32, v123
	v_mov_b32_e32 v33, v123
	v_mov_b32_e32 v50, v123
	v_mov_b32_e32 v51, v123
	v_mov_b32_e32 v52, v123
	v_mov_b32_e32 v53, v123
	v_mov_b32_e32 v54, v123
	v_mov_b32_e32 v55, v123
	v_mov_b32_e32 v56, v123
	v_mov_b32_e32 v57, v123
	v_mov_b32_e32 v58, v123
	v_mov_b32_e32 v59, v123
	v_mov_b32_e32 v60, v123
	v_mov_b32_e32 v61, v123
	v_mov_b32_e32 v62, v123
	v_mov_b32_e32 v63, v123
	v_mov_b32_e32 v64, v123
	v_mov_b32_e32 v65, v123
	v_mov_b32_e32 v2, v123
	v_mov_b32_e32 v3, v123
	v_mov_b32_e32 v4, v123
	v_mov_b32_e32 v5, v123
	v_mov_b32_e32 v6, v123
	v_mov_b32_e32 v7, v123
	v_mov_b32_e32 v8, v123
	v_mov_b32_e32 v9, v123
	v_mov_b32_e32 v10, v123
	v_mov_b32_e32 v11, v123
	v_mov_b32_e32 v12, v123
	v_mov_b32_e32 v13, v123
	v_mov_b32_e32 v14, v123
	v_mov_b32_e32 v15, v123
	v_mov_b32_e32 v16, v123
	v_mov_b32_e32 v17, v123
	v_mov_b32_e32 v34, v123
	v_mov_b32_e32 v35, v123
	v_mov_b32_e32 v36, v123
	v_mov_b32_e32 v37, v123
	v_mov_b32_e32 v38, v123
	v_mov_b32_e32 v39, v123
	v_mov_b32_e32 v40, v123
	v_mov_b32_e32 v41, v123
	v_mov_b32_e32 v42, v123
	v_mov_b32_e32 v43, v123
	v_mov_b32_e32 v44, v123
	v_mov_b32_e32 v45, v123
	v_mov_b32_e32 v46, v123
	v_mov_b32_e32 v47, v123
	v_mov_b32_e32 v48, v123
	v_mov_b32_e32 v49, v123
	s_barrier
	s_branch .LBB1_4
